# v021 + s_nop pad for the x4-store data WAR in the rope epilogue (store followed by v_mov_b64 across a branch)
# baseline (speedup 1.0000x reference)
; __device__ __forceinline__ unsigned pk2(float a, float b) { f32x2 v = {a, b}; bf16x2_t r = __builtin_convertvector(v, bf16x2_t); return __builtin_bit_cast(unsigned, r); }
;     __device__ __forceinline__ void operator()(int ui) { if (ui == slot) run(); }
;     __device__ __forceinline__ void operator()(const f32x4 (&acc)[2][2][4][2], const Unit& u, int wr, int wc, int fr, int fq) const {
;         const int row0 = u.pm * BM + wr * 64 + fr, col0 = u.pn * BM + wc * 32 + 8 * fq; const bool rot = (u.pn < 16) && (wc == 0);
; #pragma unroll
;         for (int ai = 0; ai < 2; ++ai)
; #pragma unroll
;             for (int m = 0; m < 4; ++m) { const int row = row0 + ai * HALF + m * 16; bf16_t* rowp = O + (size_t)row * ldc + col0;
;                 f32x4 cv = {1.f, 1.f, 1.f, 1.f}, sv = {0.f, 0.f, 0.f, 0.f};
;                 if (rot) { const int pos = row & (T - 1); cv = *(const f32x4*)(rc + pos * 16 + 4 * fq); sv = *(const f32x4*)(rs + pos * 16 + 4 * fq); }
; #pragma unroll
;                 for (int bj = 0; bj < 2; ++bj) { f32x4 v0 = acc[ai][bj][m][0] * sc, v1 = acc[ai][bj][m][1] * sc;
;                     if (rot) { const f32x4 a = v0, b = v1;
;                         v0[0] = a[0] * cv[0] - a[1] * sv[0]; v0[1] = a[0] * sv[0] + a[1] * cv[0]; v0[2] = a[2] * cv[1] - a[3] * sv[1]; v0[3] = a[2] * sv[1] + a[3] * cv[1];
;                         v1[0] = b[0] * cv[2] - b[1] * sv[2]; v1[1] = b[0] * sv[2] + b[1] * cv[2]; v1[2] = b[2] * cv[3] - b[3] * sv[3]; v1[3] = b[2] * sv[3] + b[3] * cv[3]; }
;                     u32x4 w; w.x = pk2(v0[0], v0[1]); w.y = pk2(v0[2], v0[3]); w.z = pk2(v1[0], v1[1]); w.w = pk2(v1[2], v1[3]);
;                     *(u32x4*)(rowp + bj * HALF) = w; } }
.LBB0_846:
	v_cvt_pk_bf16_f32 v2, v16, v17
	v_cvt_pk_bf16_f32 v3, v22, v23
	v_cvt_pk_bf16_f32 v4, v18, v19
	v_cvt_pk_bf16_f32 v5, v20, v21
	s_and_b64 vcc, exec, s[8:9]
	v_add_u32_e32 v22, 0xb0, v24
	global_store_dwordx4 v[14:15], v[2:5], off offset:256
	s_cbranch_vccnz .LBB0_848
	s_nop 0
	v_mov_b64_e32 v[2:3], v[224:225]
	v_mov_b64_e32 v[4:5], v[226:227]
	v_mov_b64_e32 v[6:7], v[228:229]
	v_mov_b64_e32 v[8:9], v[230:231]
	s_branch .LBB0_849
